# phase prologues: P10 key staging (8 serial round trips) and conv-weight staging loops unrolled so that all loads are in flight together
# baseline (speedup 1.0000x reference)
; #define LAS __attribute__((address_space(3)))
; __device__ __forceinline__ void p2_load_raw(P2Raw& R, const bf16* QKM, const bf16* VM, const float* IFb, const float* cw, int item, int tid, int lane, int wave) {
;     const int bh = item >> 8, c = item & 255, b = bh >> 2, h = bh & 3, ch = tid & 127, chan = 512 + h * 128 + ch;
; #pragma unroll
;     for (int i = 0; i < 5; ++i) { const int v = tid + 512 * i, rr = v >> 5, pc = v & 31, t = c * 64 + rr - 3;
;         v4u val = {0u, 0u, 0u, 0u};
;         if (v < 2144 && t >= 0) val = pc < 16 ? *(const v4u*)(QKM + ((size_t)b * SEQ + t) * 1024 + 512 + h * 128 + 8 * pc) : *(const v4u*)(VM + ((size_t)b * SEQ + t) * 512 + h * 128 + 8 * (pc - 16));
;         R.raw[i] = val; }
; __device__ __forceinline__ void p2_mlstm_local(const Params& P, LAS unsigned char* lds, int tid, int lane, int wave, int vb) {
;     ...
;     for (int i = tid; i < 1024; i += 512) ((LAS f32x4*)CWl)[i] = ((const f32x4*)cw)[i];
;     __syncthreads();
;     const int r = lane & 15, g = lane >> 4;
;     P2Raw pre; pre.lfi = 0.f; pre.ipi = 0.f;
;     if (vb < 2048) p2_load_raw(pre, QKM, VM, IFb, cw, vb, tid, lane, wave);
.LBB0_433:
	v_lshl_add_u64 v[14:15], v[2:3], 0, s[4:5]
	global_load_dwordx4 v[6:9], v[2:3], off
	global_load_dwordx4 v[10:13], v[14:15], off
	s_waitcnt vmcnt(1)
	ds_write_b128 v5, v[6:9]
	s_waitcnt vmcnt(0)
	ds_write_b128 v5, v[10:13] offset:8192
	s_or_b64 exec, exec, s[2:3]
	s_add_u32 s10, s26, 0x13800000
	s_addc_u32 s11, s27, 0
	s_add_u32 s41, s26, 0xf800000
	s_addc_u32 s54, s27, 0
	s_add_u32 s30, s26, 0x1700000
	s_addc_u32 s31, s27, 0
	s_cmpk_lt_i32 s72, 0x800
	s_cselect_b64 s[4:5], -1, 0
	s_and_b64 vcc, exec, s[4:5]
	v_cmp_lt_u32_e64 s[2:3], 15, v1
	v_lshlrev_b32_e32 v30, 3, v1
	v_lshrrev_b32_e32 v31, 5, v0
	s_waitcnt lgkmcnt(0)
	s_barrier
	s_cbranch_vccz .LBB0_463
	s_ashr_i32 s6, s72, 10
	s_bfe_u32 s16, s72, 0x20008
	s_lshl_b32 s0, s72, 6
	s_ashr_i32 s7, s6, 31
	s_lshl_b32 s18, s16, 7
	s_and_b32 s17, s0, 0x3fc0
	s_lshl_b64 s[8:9], s[6:7], 24
	s_add_u32 s0, s10, s8
	s_addc_u32 s1, s11, s9
	s_lshl_b32 s8, s16, 8
	s_add_u32 s8, s0, s8
	s_addc_u32 s9, s1, 0
	v_mov_b32_e32 v53, 0
	v_lshl_add_u64 v[10:11], s[8:9], 0, v[52:53]
	s_lshl_b64 s[8:9], s[6:7], 25
	s_add_u32 s8, s41, s8
	v_or_b32_e32 v6, s17, v31
	s_addc_u32 s9, s54, s9
	v_cmp_lt_u32_e32 vcc, 2, v6
	v_mov_b32_e32 v52, v53
	v_mov_b32_e32 v54, v53
	v_mov_b32_e32 v55, v53
	s_and_saveexec_b64 s[12:13], vcc
	s_cbranch_execz .LBB0_441
	v_add_u32_e32 v52, -3, v6
	s_and_saveexec_b64 s[14:15], s[2:3]
	s_xor_b64 s[14:15], exec, s[14:15]
	v_lshlrev_b64 v[2:3], 10, v[52:53]
	s_movk_i32 s20, 0xff00
	v_lshl_add_u64 v[2:3], v[10:11], 0, v[2:3]
	s_mov_b32 s21, -1
	v_lshl_add_u64 v[2:3], v[2:3], 0, s[20:21]
	s_andn2_saveexec_b64 s[14:15], s[14:15]
	s_cbranch_execz .LBB0_440
	v_lshlrev_b64 v[2:3], 11, v[52:53]
	v_lshl_add_u64 v[2:3], s[8:9], 0, v[2:3]
	s_lshl_b32 s20, s18, 1
	s_mov_b32 s21, 0
	v_lshl_add_u64 v[2:3], v[2:3], 0, s[20:21]
	v_lshlrev_b32_e32 v4, 1, v30
	v_mov_b32_e32 v5, 0
	v_lshl_add_u64 v[2:3], v[2:3], 0, v[4:5]
	s_mov_b64 s[20:21], 0x400
	v_lshl_add_u64 v[2:3], v[2:3], 0, s[20:21]

; #define LAS __attribute__((address_space(3)))
; __device__ __forceinline__ void p4_prefetch_raw(P4Pref& pf, const Params& P, int item, int tid, int lane) {
;     ...
;     for (int i = 0; i < 7; ++i) { const int v = tid + 512 * i; const int rr = v / 48, rem = v - rr * 48, seg = rem >> 4, c16 = rem & 15; const int t = c * 64 + rr - 3;
;         v4u val = {0u, 0u, 0u, 0u};
;         if (v < 3216 && t >= 0) val = (seg < 2) ? *(const v4u*)(QKM + ((size_t)b * SEQ + t) * 1024 + seg * 512 + h * 128 + 8 * c16) : *(const v4u*)(VM + ((size_t)b * SEQ + t) * 512 + h * 128 + 8 * c16);
;         pf.raw[i] = val; }
; __device__ __forceinline__ void p4_mlstm_out(const Params& P, LAS unsigned char* lds, int tid, int lane, int wave, int vb) {
;     ...
;     for (int i = tid; i < 1024; i += 512) ((LAS f32x4*)CW)[i] = ((const f32x4*)cw)[i];
;     P4Pref pf;
;     if (vb < 2048) { p4_prefetch_raw(pf, P, vb, tid, lane); p4_prefetch_cs(pf, P, vb, lane, wave); p4_prefetch_om(pf, P, vb, lane, wave); }
.LBB0_738:
	v_lshl_add_u64 v[14:15], v[2:3], 0, s[4:5]
	global_load_dwordx4 v[6:9], v[2:3], off
	global_load_dwordx4 v[10:13], v[14:15], off
	s_waitcnt vmcnt(1)
	ds_write_b128 v4, v[6:9]
	s_waitcnt vmcnt(0)
	ds_write_b128 v4, v[10:13] offset:8192
	s_or_b64 exec, exec, s[2:3]
	s_cmpk_lt_i32 s72, 0x800
	s_cselect_b64 s[2:3], -1, 0
	v_and_b32_e32 v116, 15, v0
	s_and_b64 vcc, exec, s[2:3]
	v_lshlrev_b32_e32 v46, 3, v0
	s_cbranch_vccz .LBB0_775
	s_ashr_i32 s4, s72, 10
	s_lshl_b32 s0, s72, 6
	s_ashr_i32 s5, s4, 31
	s_bfe_u32 s10, s72, 0x20008
	s_and_b32 s11, s0, 0x3fc0
	s_lshl_b64 s[6:7], s[4:5], 24
	s_add_u32 s0, s64, s6
	s_addc_u32 s1, s65, s7
	s_lshl_b32 s14, s10, 7
	s_lshl_b32 s6, s10, 8
	s_add_u32 s6, s0, s6
	v_and_b32_e32 v1, 0x78, v46
	v_mov_b32_e32 v3, 0
	s_addc_u32 s7, s1, 0
	v_lshlrev_b32_e32 v22, 1, v1
	v_mov_b32_e32 v23, v3
	v_lshl_add_u64 v[4:5], s[6:7], 0, v[22:23]
	s_mov_b64 s[6:7], 0x13800000
	v_lshl_add_u64 v[24:25], v[4:5], 0, s[6:7]
	s_lshl_b64 s[6:7], s[4:5], 25
	s_add_u32 s0, s64, s6
	v_mul_u32_u24_e32 v1, 0x556, v0
	s_addc_u32 s1, s65, s7
	v_lshrrev_b32_e32 v1, 16, v1
	s_add_u32 s6, s0, 0xf800000
	v_or_b32_e32 v6, s11, v1
	s_addc_u32 s7, s1, 0
	v_cmp_lt_u32_e32 vcc, 2, v6
	v_mov_b32_e32 v2, v3
	v_mov_b32_e32 v4, v3
	v_mov_b32_e32 v5, v3
	s_and_saveexec_b64 s[8:9], vcc
	s_cbranch_execz .LBB0_746
	s_movk_i32 s0, 0xffd0
	v_mad_i32_i24 v1, v1, s0, v0
	v_ashrrev_i32_e32 v1, 4, v1
	v_add_u32_e32 v2, -3, v6
	v_cmp_lt_i32_e32 vcc, 1, v1
	s_and_saveexec_b64 s[12:13], vcc
	s_xor_b64 s[12:13], exec, s[12:13]
	v_lshlrev_b64 v[2:3], 10, v[2:3]
	v_lshl_add_u64 v[4:5], v[24:25], 0, v[2:3]
	s_andn2_saveexec_b64 s[12:13], s[12:13]
	s_cbranch_execz .LBB0_745
	v_lshlrev_b64 v[2:3], 11, v[2:3]
	v_lshlrev_b32_e32 v4, 9, v1
	v_lshl_add_u64 v[2:3], s[6:7], 0, v[2:3]
	v_ashrrev_i32_e32 v5, 31, v4
	v_lshl_add_u64 v[2:3], v[4:5], 1, v[2:3]
	s_lshl_b32 s16, s14, 1
	s_mov_b32 s17, 0
	v_lshl_add_u64 v[2:3], v[2:3], 0, s[16:17]
	v_mov_b32_e32 v23, 0
	v_lshl_add_u64 v[4:5], v[2:3], 0, v[22:23]

; #define LAS __attribute__((address_space(3)))
; __device__ __forceinline__ void p10_topk(const Params& P, LAS unsigned char* lds, int tid, int lane, int wave, int vb) {
;     ...
;     const int h = vb & 7, wgx = vb >> 3, nwg = gridDim.x >> 3;
;     __syncthreads();
;     for (int i = tid; i < 4096; i += 512) { const int half = i >> 11, rem = i & 2047, n = rem >> 4, c = rem & 15;
;         *(LAS v4u*)(Kl + half * 17408 + n * 136 + c * 8) = *(const v4u*)((half ? K2B : K1B) + (size_t)h * 16384 + n * 128 + c * 8); }
;     __syncthreads();
.LBB0_1232:
	s_cmp_lt_i32 s86, 11
	s_cselect_b64 s[0:1], -1, 0
	s_and_b64 s[20:21], s[0:1], s[2:3]
	s_andn2_b64 vcc, exec, s[20:21]
	s_cbranch_vccnz .LBB0_1275
	s_waitcnt vmcnt(0)
	v_mov_b32_e32 v4, v0
	s_movk_i32 s0, 0x1000
	s_and_b32 s18, s72, 7
	v_cmp_gt_i32_e32 vcc, s0, v4
	s_waitcnt lgkmcnt(0)
	s_barrier
	s_and_saveexec_b64 s[2:3], vcc
	s_cbranch_execz .LBB0_1236
	s_lshl_b32 s0, s18, 15
	s_add_u32 s4, s64, s0
	s_addc_u32 s5, s65, 0
	s_add_u32 s4, s4, 0x1680000
	s_addc_u32 s5, s5, 0
	v_lshlrev_b32_e32 v1, 4, v4
	v_lshrrev_b32_e32 v2, 4, v4
	v_and_b32_e32 v3, 15, v4
	v_mul_u32_u24_e32 v2, 0x110, v2
	v_lshl_add_u32 v2, v3, 4, v2
	global_load_dwordx4 v[16:19], v1, s[4:5]
	v_add_u32_e32 v5, 0x2000, v1
	global_load_dwordx4 v[20:23], v5, s[4:5]
	v_add_u32_e32 v6, 0x4000, v1
	global_load_dwordx4 v[24:27], v6, s[4:5]
	v_add_u32_e32 v7, 0x6000, v1
	global_load_dwordx4 v[28:31], v7, s[4:5]
	v_add_u32_e32 v8, 0x40000, v1
	global_load_dwordx4 v[32:35], v8, s[4:5]
	v_add_u32_e32 v9, 0x42000, v1
	global_load_dwordx4 v[36:39], v9, s[4:5]
	v_add_u32_e32 v10, 0x44000, v1
	global_load_dwordx4 v[40:43], v10, s[4:5]
	v_add_u32_e32 v11, 0x46000, v1
	global_load_dwordx4 v[44:47], v11, s[4:5]
	s_waitcnt vmcnt(7)
	ds_write_b128 v2, v[16:19]
	s_waitcnt vmcnt(6)
	ds_write_b128 v2, v[20:23] offset:8704
	s_waitcnt vmcnt(5)
	ds_write_b128 v2, v[24:27] offset:17408
	s_waitcnt vmcnt(4)
	ds_write_b128 v2, v[28:31] offset:26112
	s_waitcnt vmcnt(3)
	ds_write_b128 v2, v[32:35] offset:34816
	s_waitcnt vmcnt(2)
	ds_write_b128 v2, v[36:39] offset:43520
	s_waitcnt vmcnt(1)
	ds_write_b128 v2, v[40:43] offset:52224
	s_waitcnt vmcnt(0)
	ds_write_b128 v2, v[44:47] offset:60928
